# v59 + grid barrier: acquire-side buffer_inv issued at arrival (waiters before the first poll, XCD leaders after their L2 write-back) so it overlaps the wait; leaders skip the unread XGEN bump
# speedup vs baseline: 1.0132x; 1.0132x over previous
; __device__ __forceinline__ unsigned xb_ld(unsigned* p)              { return __hip_atomic_load(p, __ATOMIC_RELAXED, __HIP_MEMORY_SCOPE_AGENT); }
; __device__ __forceinline__ unsigned xb_add(unsigned* p, unsigned v) { return __hip_atomic_fetch_add(p, v, __ATOMIC_RELAXED, __HIP_MEMORY_SCOPE_AGENT); }
; #define XB_SPIN(cond, bar) do { unsigned _sp = 0; while (cond) { __builtin_amdgcn_s_sleep(1); \
;     if ((++_sp & 255u) == 0u) { if (xb_ld(&(bar)[XB_TMO])) break; if (_sp > XB_SPIN_CAP) { atomicAdd(&(bar)[XB_TMO], 1u); break; } } } } while (0)
; __device__ __forceinline__ void xcd_barrier(const XcdBarrier& b) {
;     ...
;         unsigned nloc = b.st[0], nx = b.st[1];
;         if (nloc == 0u) { xcd_barrier_complete(bar, b.x, nloc, nx); b.st[0] = nloc; b.st[1] = nx; }
;         const unsigned old = xb_add(&bar[XB_XSUB(b.x)], 1u);
;         const unsigned gen = old / nloc;
;         if (old + 1u == (gen + 1u) * nloc) {
;             __builtin_amdgcn_fence(__ATOMIC_RELEASE, "agent");
;             asm volatile("s_waitcnt vmcnt(0)" ::: "memory");
;             const unsigned og = xb_add(&bar[XB_TOP], 1u);
;             const unsigned tg = og / nx;
;             if (og + 1u == (tg + 1u) * nx) xb_add(&bar[XB_TOPGEN], 1u);
;             else XB_SPIN(xb_ld(&bar[XB_TOPGEN]) == tg, bar);
;             __builtin_amdgcn_fence(__ATOMIC_ACQUIRE, "agent");
;             xb_add(&bar[XB_XGEN(b.x)], 1u);
;             asm volatile("s_waitcnt vmcnt(0)" ::: "memory");
;         } else {
;             XB_SPIN(xb_ld(&bar[XB_XGEN(b.x)]) == gen, bar);
.LBB0_162:
	s_lshl_b32 s0, s54, 8
	s_add_u32 s25, s55, s0
	s_addc_u32 s24, s56, 0
	v_mov_b32_e32 v3, s25
	v_add_co_u32_e32 v6, vcc, 0x1000, v3
	v_mov_b32_e32 v3, s24
	s_nop 0
	v_addc_co_u32_e32 v7, vcc, 0, v3, vcc
	v_mov_b32_e32 v3, 1
	flat_atomic_add v3, v[6:7], v3 offset:1024 sc0
	v_cvt_f32_u32_e32 v5, v4
	v_sub_u32_e32 v6, 0, v4
	v_rcp_iflag_f32_e32 v5, v5
	s_nop 0
	v_mul_f32_e32 v5, 0x4f7ffffe, v5
	v_cvt_u32_f32_e32 v5, v5
	v_mul_lo_u32 v6, v6, v5
	v_mul_hi_u32 v6, v5, v6
	v_add_u32_e32 v5, v5, v6
	s_waitcnt vmcnt(0) lgkmcnt(0)
	v_mul_hi_u32 v5, v3, v5
	v_mul_lo_u32 v7, v5, v4
	v_add_u32_e32 v6, 1, v3
	v_sub_u32_e32 v3, v3, v7
	v_add_u32_e32 v8, 1, v5
	v_cmp_ge_u32_e32 vcc, v3, v4
	v_sub_u32_e32 v7, v3, v4
	s_nop 0
	v_cndmask_b32_e32 v5, v5, v8, vcc
	v_cndmask_b32_e32 v3, v3, v7, vcc
	v_add_u32_e32 v7, 1, v5
	v_cmp_ge_u32_e32 vcc, v3, v4
	s_nop 1
	v_cndmask_b32_e32 v3, v5, v7, vcc
	v_mad_u64_u32 v[4:5], s[0:1], v4, v3, v[4:5]
	v_cmp_ne_u32_e32 vcc, v6, v4
	s_and_saveexec_b64 s[0:1], vcc
	s_xor_b64 s[0:1], exec, s[0:1]
	s_cbranch_execz .LBB0_175
	v_mov_b32_e32 v2, s25
	v_add_co_u32_e32 v4, vcc, 0x2000, v2
	v_mov_b32_e32 v2, s24
	s_nop 0
	v_addc_co_u32_e32 v5, vcc, 0, v2, vcc
	s_add_u32 s8, s36, 0x7500
	s_addc_u32 s9, s37, 0
	v_mov_b64_e32 v[4:5], s[8:9]
	buffer_inv sc1
	flat_load_dword v2, v[4:5] sc1
	s_waitcnt vmcnt(0) lgkmcnt(0)
	v_cmp_eq_u32_e32 vcc, v2, v3
	s_and_saveexec_b64 s[4:5], vcc
	s_cbranch_execz .LBB0_174
	s_add_u32 s6, s36, 0x4200
	s_addc_u32 s7, s37, 0
	s_mov_b32 s26, 1
	s_mov_b64 s[10:11], 0
	s_branch .LBB0_166

; __device__ __forceinline__ unsigned xb_ld(unsigned* p)              { return __hip_atomic_load(p, __ATOMIC_RELAXED, __HIP_MEMORY_SCOPE_AGENT); }
; __device__ __forceinline__ unsigned xb_add(unsigned* p, unsigned v) { return __hip_atomic_fetch_add(p, v, __ATOMIC_RELAXED, __HIP_MEMORY_SCOPE_AGENT); }
; #define XB_SPIN(cond, bar) do { unsigned _sp = 0; while (cond) { __builtin_amdgcn_s_sleep(1); \
;     if ((++_sp & 255u) == 0u) { if (xb_ld(&(bar)[XB_TMO])) break; if (_sp > XB_SPIN_CAP) { atomicAdd(&(bar)[XB_TMO], 1u); break; } } } } while (0)
; __device__ __forceinline__ void xcd_barrier(const XcdBarrier& b) {
;     ...
;         if (old + 1u == (gen + 1u) * nloc) {
;             __builtin_amdgcn_fence(__ATOMIC_RELEASE, "agent");
;             asm volatile("s_waitcnt vmcnt(0)" ::: "memory");
;             const unsigned og = xb_add(&bar[XB_TOP], 1u);
;             const unsigned tg = og / nx;
;             if (og + 1u == (tg + 1u) * nx) xb_add(&bar[XB_TOPGEN], 1u);
;             else XB_SPIN(xb_ld(&bar[XB_TOPGEN]) == tg, bar);
;             __builtin_amdgcn_fence(__ATOMIC_ACQUIRE, "agent");
;             xb_add(&bar[XB_XGEN(b.x)], 1u);
;             asm volatile("s_waitcnt vmcnt(0)" ::: "memory");
;         } else {
;             XB_SPIN(xb_ld(&bar[XB_XGEN(b.x)]) == gen, bar);
.LBB0_174:
	s_or_b64 exec, exec, s[4:5]
	s_waitcnt vmcnt(0) lgkmcnt(0)
	s_waitcnt vmcnt(0)
.LBB0_175:
	s_andn2_saveexec_b64 s[0:1], s[0:1]
	s_cbranch_execz .LBB0_191
	v_mov_b32_e32 v3, s36
	v_add_co_u32_e32 v4, vcc, 0x7000, v3
	v_mov_b32_e32 v3, s37
	buffer_wbl2 sc1
	s_waitcnt vmcnt(0)
	buffer_inv sc1
	v_addc_co_u32_e32 v5, vcc, 0, v3, vcc
	v_mov_b32_e32 v3, 1
	flat_atomic_add v3, v[4:5], v3 offset:1024 sc0
	v_cvt_f32_u32_e32 v4, v2
	v_sub_u32_e32 v5, 0, v2
	s_add_u32 s0, s36, 0x7500
	s_addc_u32 s1, s37, 0
	v_rcp_iflag_f32_e32 v4, v4
	s_mov_b64 s[6:7], -1
	v_mul_f32_e32 v4, 0x4f7ffffe, v4
	v_cvt_u32_f32_e32 v4, v4
	v_mul_lo_u32 v5, v5, v4
	v_mul_hi_u32 v5, v4, v5
	v_add_u32_e32 v4, v4, v5
	s_waitcnt vmcnt(0) lgkmcnt(0)
	v_mul_hi_u32 v4, v3, v4
	v_mul_lo_u32 v6, v4, v2
	v_add_u32_e32 v5, 1, v3
	v_sub_u32_e32 v3, v3, v6
	v_add_u32_e32 v7, 1, v4
	v_cmp_ge_u32_e32 vcc, v3, v2
	v_sub_u32_e32 v6, v3, v2
	s_nop 0
	v_cndmask_b32_e32 v4, v4, v7, vcc
	v_cndmask_b32_e32 v3, v3, v6, vcc
	v_add_u32_e32 v6, 1, v4
	v_cmp_ge_u32_e32 vcc, v3, v2
	s_nop 1
	v_cndmask_b32_e32 v4, v4, v6, vcc
	v_mad_u64_u32 v[2:3], s[4:5], v2, v4, v[2:3]
	v_cmp_ne_u32_e32 vcc, v5, v2
	v_mov_b64_e32 v[2:3], s[0:1]
	s_and_saveexec_b64 s[4:5], vcc
	s_cbranch_execz .LBB0_188
	v_mov_b64_e32 v[2:3], s[0:1]
	flat_load_dword v2, v[2:3] sc1
	s_mov_b64 s[10:11], 0
	s_waitcnt vmcnt(0) lgkmcnt(0)
	v_cmp_eq_u32_e32 vcc, v2, v4
	s_and_saveexec_b64 s[8:9], vcc
	s_cbranch_execz .LBB0_187
	s_add_u32 s6, s36, 0x4200
	s_addc_u32 s7, s37, 0
	s_mov_b32 s22, 1
	s_branch .LBB0_180

; __device__ __forceinline__ unsigned xb_ld(unsigned* p)              { return __hip_atomic_load(p, __ATOMIC_RELAXED, __HIP_MEMORY_SCOPE_AGENT); }
; __device__ __forceinline__ unsigned xb_add(unsigned* p, unsigned v) { return __hip_atomic_fetch_add(p, v, __ATOMIC_RELAXED, __HIP_MEMORY_SCOPE_AGENT); }
; #define XB_SPIN(cond, bar) do { unsigned _sp = 0; while (cond) { __builtin_amdgcn_s_sleep(1); \
;     if ((++_sp & 255u) == 0u) { if (xb_ld(&(bar)[XB_TMO])) break; if (_sp > XB_SPIN_CAP) { atomicAdd(&(bar)[XB_TMO], 1u); break; } } } } while (0)
; __device__ __forceinline__ void xcd_barrier(const XcdBarrier& b) {
;     ...
;             if (og + 1u == (tg + 1u) * nx) xb_add(&bar[XB_TOPGEN], 1u);
;             else XB_SPIN(xb_ld(&bar[XB_TOPGEN]) == tg, bar);
;             __builtin_amdgcn_fence(__ATOMIC_ACQUIRE, "agent");
;             xb_add(&bar[XB_XGEN(b.x)], 1u);
;             asm volatile("s_waitcnt vmcnt(0)" ::: "memory");
.LBB0_190:
	s_or_b64 exec, exec, s[0:1]
	v_mov_b32_e32 v2, s25
	v_add_co_u32_e32 v2, vcc, 0x2000, v2
	v_mov_b32_e32 v3, s24
	s_nop 0
	v_addc_co_u32_e32 v3, vcc, 0, v3, vcc
	v_mov_b32_e32 v4, 1
	s_waitcnt vmcnt(0) lgkmcnt(0)
	s_waitcnt vmcnt(0)
